# defer2 (P2 deferred tiles) + removed compiler vmcnt(0) at P5a/P5r/P6 unit heads (stores left outstanding under the first two counted waits)
# baseline (speedup 1.0000x reference)
; #define LAS __attribute__((address_space(3)))
; #define PG8_STAGEA(bufoff, gbase, h) PG8_STAGE2(bufoff, gbase, voffA[h][0], voffA[h][1])
; #define PG8_LDA(dst, b, h) do { _Pragma("unroll") for (int m = 0; m < 4; ++m) _Pragma("unroll") for (int k = 0; k < 2; ++k) dst[m][k] = *(const LAS bf16x8*)(lds + PG8_SA(b, h) + aoff + m * 2048 + k * 1024); } while (0)
; #define PG8_LDB(dst, b, h) do { _Pragma("unroll") for (int n = 0; n < 2; ++n) _Pragma("unroll") for (int k = 0; k < 2; ++k) dst[n][k] = *(const LAS bf16x8*)(lds + PG8_SB(b, h) + boff + n * 2048 + k * 1024); } while (0)
; #define PG8_WAIT_K0() do { if (EST > 0 && t == 0 && ui > 0) asm volatile("s_waitcnt vmcnt(%0)" :: "n"((HM ? 6 : 8) + EST) : "memory"); else PG8_WAIT_K(); } while (0)
; #define PG8_WAIT_L(n) asm volatile("s_waitcnt lgkmcnt(" #n ")" ::: "memory")
; #define PG8_BAR __builtin_amdgcn_s_barrier()
; #define PG8_SCHED __builtin_amdgcn_sched_barrier(0)
;     ...
;             PG8_LDB(B0, 0, 0); PG8_LDB(B1, 0, 1); PG8_SCHED; PG8_LDA(At, 0, 0); if constexpr (!HM) PG8_STAGEA(PG8_SA(1, 1), a1, 1);
;             if constexpr (Sched::kGather) { if (last && has_next) { const u32x4 tn = *(const LAS u32x4*)(S.aux + tid * 16); voffA[0][0] = tn.x; voffA[0][1] = tn.y; voffA[1][0] = tn.z; voffA[1][1] = tn.w; } }
;             PG8_WAIT_K0(); PG8_WAIT_L(0); PG8_BAR; PG8_MMA(0, 0, At, B0); PG8_MMA(0, 1, At, B1); PG8_BAR; PG8_SCHED;
.LBB0_574:
	ds_read_b128 v[18:21], v167
	ds_read_b128 v[22:25], v167 offset:1024
	ds_read_b128 v[26:29], v167 offset:2048
	ds_read_b128 v[30:33], v167 offset:3072
	ds_read_b128 v[2:5], v168
	ds_read_b128 v[6:9], v168 offset:1024
	ds_read_b128 v[10:13], v168 offset:2048
	ds_read_b128 v[14:17], v168 offset:3072
	s_cmp_lg_u32 s42, 0
	s_cselect_b64 s[42:43], -1, 0
	s_add_u32 s44, s38, 0x80
	s_addc_u32 s45, s39, 0
	ds_read_b128 v[74:77], v169
	ds_read_b128 v[78:81], v169 offset:1024
	ds_read_b128 v[82:85], v169 offset:2048
	ds_read_b128 v[90:93], v169 offset:3072
	ds_read_b128 v[94:97], v169 offset:4096
	ds_read_b128 v[98:101], v169 offset:5120
	ds_read_b128 v[70:73], v169 offset:6144
	ds_read_b128 v[86:89], v169 offset:7168
	s_mov_b32 s29, m0
	s_mov_b32 m0, s68
	s_nop 0
	global_load_lds_dwordx4 v162, s[44:45]
	s_mov_b32 m0, s29
	s_and_b64 vcc, exec, s[42:43]
	s_mov_b32 s29, m0
	s_mov_b32 m0, s69
	s_nop 0
	global_load_lds_dwordx4 v163, s[44:45]
	s_mov_b32 m0, s29
	s_cbranch_vccz .LBB0_587
	s_waitcnt vmcnt(24)
	s_cbranch_execnz .LBB0_577

; #define LAS __attribute__((address_space(3)))
; #define PG8_STAGEA(bufoff, gbase, h) PG8_STAGE2(bufoff, gbase, voffA[h][0], voffA[h][1])
; #define PG8_LDA(dst, b, h) do { _Pragma("unroll") for (int m = 0; m < 4; ++m) _Pragma("unroll") for (int k = 0; k < 2; ++k) dst[m][k] = *(const LAS bf16x8*)(lds + PG8_SA(b, h) + aoff + m * 2048 + k * 1024); } while (0)
; #define PG8_LDB(dst, b, h) do { _Pragma("unroll") for (int n = 0; n < 2; ++n) _Pragma("unroll") for (int k = 0; k < 2; ++k) dst[n][k] = *(const LAS bf16x8*)(lds + PG8_SB(b, h) + boff + n * 2048 + k * 1024); } while (0)
; #define PG8_WAIT_K0() do { if (EST > 0 && t == 0 && ui > 0) asm volatile("s_waitcnt vmcnt(%0)" :: "n"((HM ? 6 : 8) + EST) : "memory"); else PG8_WAIT_K(); } while (0)
; #define PG8_WAIT_L(n) asm volatile("s_waitcnt lgkmcnt(" #n ")" ::: "memory")
; #define PG8_BAR __builtin_amdgcn_s_barrier()
; #define PG8_SCHED __builtin_amdgcn_sched_barrier(0)
;     ...
;             PG8_LDB(B0, 0, 0); PG8_LDB(B1, 0, 1); PG8_SCHED; PG8_LDA(At, 0, 0); if constexpr (!HM) PG8_STAGEA(PG8_SA(1, 1), a1, 1);
;             if constexpr (Sched::kGather) { if (last && has_next) { const u32x4 tn = *(const LAS u32x4*)(S.aux + tid * 16); voffA[0][0] = tn.x; voffA[0][1] = tn.y; voffA[1][0] = tn.z; voffA[1][1] = tn.w; } }
;             PG8_WAIT_K0(); PG8_WAIT_L(0); PG8_BAR; PG8_MMA(0, 0, At, B0); PG8_MMA(0, 1, At, B1); PG8_BAR; PG8_SCHED;
.LBB0_604:
	ds_read_b128 v[18:21], v180
	ds_read_b128 v[22:25], v180 offset:1024
	ds_read_b128 v[26:29], v180 offset:2048
	ds_read_b128 v[30:33], v180 offset:3072
	ds_read_b128 v[2:5], v181
	ds_read_b128 v[6:9], v181 offset:1024
	ds_read_b128 v[10:13], v181 offset:2048
	ds_read_b128 v[14:17], v181 offset:3072
	s_cmp_lg_u32 s28, 0
	s_cselect_b64 s[28:29], -1, 0
	s_add_u32 s30, s24, 0x80
	s_addc_u32 s31, s25, 0
	ds_read_b128 v[70:73], v182
	ds_read_b128 v[82:85], v182 offset:1024
	ds_read_b128 v[86:89], v182 offset:2048
	ds_read_b128 v[98:101], v182 offset:3072
	ds_read_b128 v[90:93], v182 offset:4096
	ds_read_b128 v[94:97], v182 offset:5120
	ds_read_b128 v[74:77], v182 offset:6144
	ds_read_b128 v[78:81], v182 offset:7168
	s_mov_b32 s17, m0
	s_mov_b32 m0, s53
	s_nop 0
	global_load_lds_dwordx4 v175, s[30:31]
	s_mov_b32 m0, s17
	s_and_b64 vcc, exec, s[28:29]
	s_mov_b32 s17, m0
	s_mov_b32 m0, s54
	s_nop 0
	global_load_lds_dwordx4 v176, s[30:31]
	s_mov_b32 m0, s17
	s_cbranch_vccz .LBB0_617
	s_waitcnt vmcnt(24)
	s_cbranch_execnz .LBB0_607

; #define LAS __attribute__((address_space(3)))
; #define PG8_STAGEA(bufoff, gbase, h) PG8_STAGE2(bufoff, gbase, voffA[h][0], voffA[h][1])
; #define PG8_LDA(dst, b, h) do { _Pragma("unroll") for (int m = 0; m < 4; ++m) _Pragma("unroll") for (int k = 0; k < 2; ++k) dst[m][k] = *(const LAS bf16x8*)(lds + PG8_SA(b, h) + aoff + m * 2048 + k * 1024); } while (0)
; #define PG8_LDB(dst, b, h) do { _Pragma("unroll") for (int n = 0; n < 2; ++n) _Pragma("unroll") for (int k = 0; k < 2; ++k) dst[n][k] = *(const LAS bf16x8*)(lds + PG8_SB(b, h) + boff + n * 2048 + k * 1024); } while (0)
; #define PG8_WAIT_K0() do { if (EST > 0 && t == 0 && ui > 0) asm volatile("s_waitcnt vmcnt(%0)" :: "n"((HM ? 6 : 8) + EST) : "memory"); else PG8_WAIT_K(); } while (0)
; #define PG8_WAIT_L(n) asm volatile("s_waitcnt lgkmcnt(" #n ")" ::: "memory")
; #define PG8_BAR __builtin_amdgcn_s_barrier()
; #define PG8_SCHED __builtin_amdgcn_sched_barrier(0)
;     ...
;             PG8_LDB(B0, 0, 0); PG8_LDB(B1, 0, 1); PG8_SCHED; PG8_LDA(At, 0, 0); if constexpr (!HM) PG8_STAGEA(PG8_SA(1, 1), a1, 1);
;             if constexpr (Sched::kGather) { if (last && has_next) { const u32x4 tn = *(const LAS u32x4*)(S.aux + tid * 16); voffA[0][0] = tn.x; voffA[0][1] = tn.y; voffA[1][0] = tn.z; voffA[1][1] = tn.w; } }
;             PG8_WAIT_K0(); PG8_WAIT_L(0); PG8_BAR; PG8_MMA(0, 0, At, B0); PG8_MMA(0, 1, At, B1); PG8_BAR; PG8_SCHED;
.LBB0_691:
	ds_read_b128 v[18:21], v208
	ds_read_b128 v[22:25], v208 offset:1024
	ds_read_b128 v[26:29], v208 offset:2048
	ds_read_b128 v[30:33], v208 offset:3072
	s_waitcnt lgkmcnt(4)
	ds_read_b128 v[2:5], v209
	ds_read_b128 v[6:9], v209 offset:1024
	ds_read_b128 v[10:13], v209 offset:2048
	ds_read_b128 v[14:17], v209 offset:3072
	s_cmp_lg_u32 s28, 0
	s_cselect_b64 s[28:29], -1, 0
	s_add_u32 s36, s30, 0x80
	s_addc_u32 s37, s31, 0
	ds_read_b128 v[74:77], v210
	ds_read_b128 v[82:85], v210 offset:1024
	ds_read_b128 v[90:93], v210 offset:2048
	ds_read_b128 v[98:101], v210 offset:3072
	ds_read_b128 v[86:89], v210 offset:4096
	ds_read_b128 v[94:97], v210 offset:5120
	ds_read_b128 v[70:73], v210 offset:6144
	ds_read_b128 v[78:81], v210 offset:7168
	s_mov_b32 s19, m0
	s_mov_b32 m0, s58
	s_nop 0
	global_load_lds_dwordx4 v203, s[36:37]
	s_mov_b32 m0, s19
	s_and_b64 vcc, exec, s[28:29]
	s_mov_b32 s19, m0
	s_mov_b32 m0, s59
	s_nop 0
	global_load_lds_dwordx4 v204, s[36:37]
	s_mov_b32 m0, s19
	s_cbranch_vccz .LBB0_720
	s_waitcnt vmcnt(40)
	s_cbranch_execnz .LBB0_694
